# v13: L1 role remap (singles+riders dispatched before empty blocks) + final_kernel hoisted W_out loads and scalar loads
# speedup vs baseline: 1.0287x; 1.0079x over previous
_Z12final_kernelPKDF16_PKfS2_Pf:
	s_load_dwordx4 s[4:7], s[0:1], 0x0
	s_load_dwordx4 s[24:27], s[0:1], 0x10
	v_and_b32_e32 v8, 63, v0
	v_lshrrev_b32_e32 v0, 6, v0
	v_lshl_or_b32 v4, s2, 2, v0
	v_ashrrev_i32_e32 v5, 31, v4
	v_lshlrev_b64 v[0:1], 11, v[4:5]
	s_waitcnt lgkmcnt(0)
	s_load_dwordx2 s[28:29], s[24:25], 0x0
	v_lshl_add_u64 v[0:1], s[4:5], 0, v[0:1]
	v_lshlrev_b32_e32 v2, 4, v8
	v_mov_b32_e32 v3, 0
	v_lshl_add_u64 v[6:7], v[0:1], 0, v[2:3]
	global_load_dwordx4 v[10:13], v[6:7], off
	v_lshlrev_b32_e32 v5, 6, v8
	global_load_dwordx4 v[14:17], v5, s[6:7]
	global_load_dwordx4 v[18:21], v5, s[6:7] offset:16
	global_load_dwordx4 v[22:25], v5, s[6:7] offset:32
	global_load_dwordx4 v[26:29], v5, s[6:7] offset:48
	global_load_dwordx4 v[0:3], v[6:7], off offset:1024
	v_lshlrev_b32_e32 v5, 3, v8
	s_movk_i32 s4, 0x3e9
	v_or_b32_e32 v62, 0x200, v5
	v_cmp_gt_u32_e64 s[8:9], s4, v62
	v_min_u32_e32 v62, 0x3e8, v62
	v_lshlrev_b32_e32 v62, 3, v62
	global_load_dwordx2 v[46:47], v62, s[6:7]
	v_or_b32_e32 v62, 0x201, v5
	v_cmp_gt_u32_e64 s[10:11], s4, v62
	v_min_u32_e32 v62, 0x3e8, v62
	v_lshlrev_b32_e32 v62, 3, v62
	global_load_dwordx2 v[48:49], v62, s[6:7]
	v_or_b32_e32 v62, 0x202, v5
	v_cmp_gt_u32_e64 s[12:13], s4, v62
	v_min_u32_e32 v62, 0x3e8, v62
	v_lshlrev_b32_e32 v62, 3, v62
	global_load_dwordx2 v[50:51], v62, s[6:7]
	v_or_b32_e32 v62, 0x203, v5
	v_cmp_gt_u32_e64 s[14:15], s4, v62
	v_min_u32_e32 v62, 0x3e8, v62
	v_lshlrev_b32_e32 v62, 3, v62
	global_load_dwordx2 v[52:53], v62, s[6:7]
	v_or_b32_e32 v62, 0x204, v5
	v_cmp_gt_u32_e64 s[16:17], s4, v62
	v_min_u32_e32 v62, 0x3e8, v62
	v_lshlrev_b32_e32 v62, 3, v62
	global_load_dwordx2 v[54:55], v62, s[6:7]
	v_or_b32_e32 v62, 0x205, v5
	v_cmp_gt_u32_e64 s[18:19], s4, v62
	v_min_u32_e32 v62, 0x3e8, v62
	v_lshlrev_b32_e32 v62, 3, v62
	global_load_dwordx2 v[56:57], v62, s[6:7]
	v_or_b32_e32 v62, 0x206, v5
	v_cmp_gt_u32_e64 s[20:21], s4, v62
	v_min_u32_e32 v62, 0x3e8, v62
	v_lshlrev_b32_e32 v62, 3, v62
	global_load_dwordx2 v[58:59], v62, s[6:7]
	v_or_b32_e32 v62, 0x207, v5
	v_cmp_gt_u32_e64 s[22:23], s4, v62
	v_min_u32_e32 v62, 0x3e8, v62
	v_lshlrev_b32_e32 v62, 3, v62
	global_load_dwordx2 v[60:61], v62, s[6:7]
	v_or_b32_e32 v9, 0x200, v5
	v_cmp_gt_u32_e32 vcc, s4, v9
	s_waitcnt vmcnt(13)
	v_cvt_f32_f16_sdwa v7, v10 dst_sel:DWORD dst_unused:UNUSED_PAD src0_sel:WORD_1
	v_cvt_f32_f16_e32 v6, v10
	v_cvt_f32_f16_e32 v30, v12
	v_cvt_f32_f16_e32 v32, v13
	v_cvt_f32_f16_e32 v10, v11
	v_cvt_f32_f16_sdwa v11, v11 dst_sel:DWORD dst_unused:UNUSED_PAD src0_sel:WORD_1
	v_cvt_f32_f16_sdwa v31, v12 dst_sel:DWORD dst_unused:UNUSED_PAD src0_sel:WORD_1
	v_cvt_f32_f16_sdwa v33, v13 dst_sel:DWORD dst_unused:UNUSED_PAD src0_sel:WORD_1
	v_max_f32_e32 v7, 0, v7
	v_max_f32_e32 v6, 0, v6
	v_max_f32_e32 v12, 0, v30
	v_max_f32_e32 v30, 0, v32
	s_waitcnt vmcnt(12)
	v_mul_f32_e32 v32, v7, v16
	v_mov_b32_e32 v16, v15
	v_max_f32_e32 v11, 0, v11
	v_mul_f32_e32 v14, v6, v14
	v_pk_mul_f32 v[6:7], v[6:7], v[16:17]
	v_max_f32_e32 v10, 0, v10
	s_waitcnt vmcnt(11)
	v_mul_f32_e32 v34, v11, v20
	v_mov_b32_e32 v20, v19
	v_mov_b32_e32 v15, v6
	v_max_f32_e32 v13, 0, v31
	v_max_f32_e32 v31, 0, v33
	v_mul_f32_e32 v18, v10, v18
	v_pk_mul_f32 v[10:11], v[10:11], v[20:21]
	v_mov_b32_e32 v33, v7
	v_pk_add_f32 v[6:7], v[14:15], 0 op_sel_hi:[1,0]
	s_waitcnt vmcnt(10)
	v_mul_f32_e32 v36, v13, v24
	v_mov_b32_e32 v24, v23
	v_mov_b32_e32 v19, v10
	v_pk_add_f32 v[6:7], v[6:7], v[32:33]
	v_mul_f32_e32 v22, v12, v22
	v_pk_mul_f32 v[12:13], v[12:13], v[24:25]
	v_mov_b32_e32 v35, v11
	v_pk_add_f32 v[6:7], v[6:7], v[18:19]
	s_waitcnt vmcnt(9)
	v_mul_f32_e32 v38, v31, v28
	v_mov_b32_e32 v28, v27
	v_mov_b32_e32 v23, v12
	v_pk_add_f32 v[6:7], v[6:7], v[34:35]
	v_pk_mul_f32 v[16:17], v[30:31], v[28:29]
	v_mov_b32_e32 v37, v13
	v_pk_add_f32 v[6:7], v[6:7], v[22:23]
	v_mul_f32_e32 v26, v30, v26
	v_mov_b32_e32 v27, v16
	v_pk_add_f32 v[6:7], v[6:7], v[36:37]
	v_mov_b32_e32 v39, v17
	v_pk_add_f32 v[6:7], v[6:7], v[26:27]
	s_nop 0
	v_pk_add_f32 v[6:7], v[6:7], v[38:39]
	s_waitcnt vmcnt(8)
	v_cvt_f32_f16_e32 v30, v0
	v_cvt_f32_f16_sdwa v32, v0 dst_sel:DWORD dst_unused:UNUSED_PAD src0_sel:WORD_1
	v_cvt_f32_f16_e32 v34, v1
	v_cvt_f32_f16_sdwa v36, v1 dst_sel:DWORD dst_unused:UNUSED_PAD src0_sel:WORD_1
	v_cvt_f32_f16_e32 v38, v2
	v_cvt_f32_f16_sdwa v40, v2 dst_sel:DWORD dst_unused:UNUSED_PAD src0_sel:WORD_1
	v_cvt_f32_f16_e32 v42, v3
	v_cvt_f32_f16_sdwa v44, v3 dst_sel:DWORD dst_unused:UNUSED_PAD src0_sel:WORD_1
	v_max_f32_e32 v30, 0, v30
	v_max_f32_e32 v32, 0, v32
	v_max_f32_e32 v34, 0, v34
	v_max_f32_e32 v36, 0, v36
	v_max_f32_e32 v38, 0, v38
	v_max_f32_e32 v40, 0, v40
	v_max_f32_e32 v42, 0, v42
	v_max_f32_e32 v44, 0, v44
	v_cndmask_b32_e64 v30, 0, v30, s[8:9]
	v_cndmask_b32_e64 v32, 0, v32, s[10:11]
	v_cndmask_b32_e64 v34, 0, v34, s[12:13]
	v_cndmask_b32_e64 v36, 0, v36, s[14:15]
	v_cndmask_b32_e64 v38, 0, v38, s[16:17]
	v_cndmask_b32_e64 v40, 0, v40, s[18:19]
	v_cndmask_b32_e64 v42, 0, v42, s[20:21]
	v_cndmask_b32_e64 v44, 0, v44, s[22:23]
	s_waitcnt vmcnt(7)
	v_pk_fma_f32 v[6:7], v[30:31], v[46:47], v[6:7] op_sel_hi:[0,1,1]
	s_waitcnt vmcnt(6)
	v_pk_fma_f32 v[6:7], v[32:33], v[48:49], v[6:7] op_sel_hi:[0,1,1]
	s_waitcnt vmcnt(5)
	v_pk_fma_f32 v[6:7], v[34:35], v[50:51], v[6:7] op_sel_hi:[0,1,1]
	s_waitcnt vmcnt(4)
	v_pk_fma_f32 v[6:7], v[36:37], v[52:53], v[6:7] op_sel_hi:[0,1,1]
	s_waitcnt vmcnt(3)
	v_pk_fma_f32 v[6:7], v[38:39], v[54:55], v[6:7] op_sel_hi:[0,1,1]
	s_waitcnt vmcnt(2)
	v_pk_fma_f32 v[6:7], v[40:41], v[56:57], v[6:7] op_sel_hi:[0,1,1]
	s_waitcnt vmcnt(1)
	v_pk_fma_f32 v[6:7], v[42:43], v[58:59], v[6:7] op_sel_hi:[0,1,1]
	s_waitcnt vmcnt(0)
	v_pk_fma_f32 v[6:7], v[44:45], v[60:61], v[6:7] op_sel_hi:[0,1,1]
	v_mbcnt_lo_u32_b32 v0, -1, 0
	v_mbcnt_hi_u32_b32 v5, -1, v0
	v_and_b32_e32 v0, 64, v5
	v_add_u32_e32 v9, 64, v0
	v_xor_b32_e32 v0, 32, v5
	v_cmp_lt_i32_e32 vcc, v0, v9
	v_xor_b32_e32 v2, 16, v5
	s_nop 0
	v_cndmask_b32_e32 v0, v5, v0, vcc
	v_lshlrev_b32_e32 v1, 2, v0
	ds_bpermute_b32 v0, v1, v6
	ds_bpermute_b32 v1, v1, v7
	v_cmp_lt_i32_e32 vcc, v2, v9
	s_waitcnt lgkmcnt(0)
	v_pk_add_f32 v[0:1], v[6:7], v[0:1]
	v_cndmask_b32_e32 v2, v5, v2, vcc
	v_lshlrev_b32_e32 v3, 2, v2
	ds_bpermute_b32 v2, v3, v0
	ds_bpermute_b32 v3, v3, v1
	v_xor_b32_e32 v6, 8, v5
	v_cmp_lt_i32_e32 vcc, v6, v9
	s_waitcnt lgkmcnt(0)
	v_pk_add_f32 v[0:1], v[0:1], v[2:3]
	v_cndmask_b32_e32 v6, v5, v6, vcc
	v_lshlrev_b32_e32 v6, 2, v6
	ds_bpermute_b32 v2, v6, v0
	ds_bpermute_b32 v3, v6, v1
	v_xor_b32_e32 v6, 4, v5
	v_cmp_lt_i32_e32 vcc, v6, v9
	s_waitcnt lgkmcnt(0)
	v_pk_add_f32 v[0:1], v[0:1], v[2:3]
	v_cndmask_b32_e32 v6, v5, v6, vcc
	v_lshlrev_b32_e32 v6, 2, v6
	ds_bpermute_b32 v2, v6, v0
	ds_bpermute_b32 v3, v6, v1
	v_xor_b32_e32 v6, 2, v5
	v_cmp_lt_i32_e32 vcc, v6, v9
	s_waitcnt lgkmcnt(0)
	v_pk_add_f32 v[0:1], v[0:1], v[2:3]
	v_cndmask_b32_e32 v6, v5, v6, vcc
	v_lshlrev_b32_e32 v6, 2, v6
	ds_bpermute_b32 v2, v6, v0
	ds_bpermute_b32 v3, v6, v1
	s_waitcnt lgkmcnt(0)
	v_pk_add_f32 v[0:1], v[0:1], v[2:3]
	v_xor_b32_e32 v2, 1, v5
	v_cmp_lt_i32_e32 vcc, v2, v9
	s_nop 1
	v_cndmask_b32_e32 v2, v5, v2, vcc
	v_lshlrev_b32_e32 v3, 2, v2
	ds_bpermute_b32 v2, v3, v0
	ds_bpermute_b32 v3, v3, v1
	v_cmp_eq_u32_e32 vcc, 0, v8
	s_and_saveexec_b64 s[2:3], vcc
	s_cbranch_execz .LBB1_18
	s_waitcnt lgkmcnt(0)
	v_pk_add_f32 v[0:1], v[0:1], v[2:3]
	v_lshlrev_b32_e32 v4, 1, v4
	s_mov_b32 s0, 0x3fb8aa3b
	s_mov_b32 s1, 0xc2ce8ed0
	s_waitcnt lgkmcnt(0)
	v_pk_add_f32 v[0:1], v[0:1], s[28:29]
	s_nop 0
	v_max_f32_e32 v6, v0, v1
	v_sub_f32_e32 v2, v0, v6
	v_mul_f32_e32 v3, 0x3fb8aa3b, v2
	v_fma_f32 v5, v2, s0, -v3
	v_rndne_f32_e32 v7, v3
	v_fmac_f32_e32 v5, 0x32a5705f, v2
	v_sub_f32_e32 v3, v3, v7
	v_add_f32_e32 v3, v3, v5
	v_cvt_i32_f32_e32 v7, v7
	v_exp_f32_e32 v3, v3
	v_sub_f32_e32 v8, v1, v6
	s_mov_b32 s4, 0x42b17218
	v_cmp_ngt_f32_e32 vcc, s1, v2
	v_ldexp_f32 v3, v3, v7
	v_mul_f32_e32 v7, 0x3fb8aa3b, v8
	v_fma_f32 v9, v8, s0, -v7
	v_rndne_f32_e32 v10, v7
	v_fmac_f32_e32 v9, 0x32a5705f, v8
	v_sub_f32_e32 v7, v7, v10
	v_add_f32_e32 v7, v7, v9
	v_exp_f32_e32 v7, v7
	v_cvt_i32_f32_e32 v9, v10
	v_cndmask_b32_e32 v3, 0, v3, vcc
	v_mov_b32_e32 v10, 0x7f800000
	v_cmp_nlt_f32_e32 vcc, s4, v2
	s_mov_b32 s0, 0x800000
	v_ashrrev_i32_e32 v5, 31, v4
	v_cndmask_b32_e32 v2, v10, v3, vcc
	v_ldexp_f32 v3, v7, v9
	v_cmp_ngt_f32_e32 vcc, s1, v8
	s_mov_b32 s1, 0x3f317217
	s_nop 0
	v_cndmask_b32_e32 v3, 0, v3, vcc
	v_cmp_nlt_f32_e32 vcc, s4, v8
	s_nop 1
	v_cndmask_b32_e32 v3, v10, v3, vcc
	v_add_f32_e32 v2, v2, v3
	v_cmp_gt_f32_e32 vcc, s0, v2
	s_mov_b32 s0, 0x7f800000
	s_nop 0
	v_cndmask_b32_e64 v3, 0, 32, vcc
	v_ldexp_f32 v2, v2, v3
	v_log_f32_e32 v7, v2
	v_lshl_add_u64 v[2:3], v[4:5], 2, s[26:27]
	v_mov_b32_e32 v5, 0x41b17218
	v_cndmask_b32_e32 v5, 0, v5, vcc
	v_mul_f32_e32 v4, 0x3f317217, v7
	v_fma_f32 v4, v7, s1, -v4
	v_fmamk_f32 v4, v7, 0x3377d1cf, v4
	v_fmac_f32_e32 v4, 0x3f317217, v7
	v_cmp_lt_f32_e64 s[0:1], |v7|, s0
	s_nop 1
	v_cndmask_b32_e64 v4, v7, v4, s[0:1]
	v_sub_f32_e32 v4, v4, v5
	v_add_f32_e32 v4, v6, v4
	v_pk_add_f32 v[0:1], v[0:1], v[4:5] op_sel_hi:[1,0] neg_lo:[0,1] neg_hi:[0,1]
	global_store_dwordx2 v[2:3], v[0:1], off

	.amdhsa_kernel _Z12final_kernelPKDF16_PKfS2_Pf
		.amdhsa_group_segment_fixed_size 0
		.amdhsa_private_segment_fixed_size 0
		.amdhsa_kernarg_size 32
		.amdhsa_user_sgpr_count 2
		.amdhsa_user_sgpr_dispatch_ptr 0
		.amdhsa_user_sgpr_queue_ptr 0
		.amdhsa_user_sgpr_kernarg_segment_ptr 1
		.amdhsa_user_sgpr_dispatch_id 0
		.amdhsa_user_sgpr_kernarg_preload_length 0
		.amdhsa_user_sgpr_kernarg_preload_offset 0
		.amdhsa_user_sgpr_private_segment_size 0
		.amdhsa_uses_dynamic_stack 0
		.amdhsa_enable_private_segment 0
		.amdhsa_system_sgpr_workgroup_id_x 1
		.amdhsa_system_sgpr_workgroup_id_y 0
		.amdhsa_system_sgpr_workgroup_id_z 0
		.amdhsa_system_sgpr_workgroup_info 0
		.amdhsa_system_vgpr_workitem_id 0
		.amdhsa_next_free_vgpr 64
		.amdhsa_next_free_sgpr 30
		.amdhsa_accum_offset 64
		.amdhsa_reserve_vcc 1
		.amdhsa_float_round_mode_32 0
		.amdhsa_float_round_mode_16_64 0
		.amdhsa_float_denorm_mode_32 3
		.amdhsa_float_denorm_mode_16_64 3
		.amdhsa_dx10_clamp 1
		.amdhsa_ieee_mode 1
		.amdhsa_fp16_overflow 0
		.amdhsa_tg_split 0
		.amdhsa_exception_fp_ieee_invalid_op 0
		.amdhsa_exception_fp_denorm_src 0
		.amdhsa_exception_fp_ieee_div_zero 0
		.amdhsa_exception_fp_ieee_overflow 0
		.amdhsa_exception_fp_ieee_underflow 0
		.amdhsa_exception_fp_ieee_inexact 0
		.amdhsa_exception_int_div_zero 0
	.end_amdhsa_kernel

_Z16gemm_glds_kernelILi2EEvPKDF16_PDF16_PKiS4_S1_S1_PKfiS6_Pc:
	s_mov_b64 s[44:45], s[0:1]
	s_mov_b32 s46, s2
	s_mov_b32 s47, 0
	s_cmp_lt_u32 s2, 0x100
	s_cbranch_scc1 .Lrm_done
	s_cmp_gt_u32 s2, 0x21f
	s_cbranch_scc1 .LBB2_14
	s_add_u32 s2, s2, 0x100
	s_mov_b32 s46, s2
.Lrm_done:
	v_mov_b32_e32 v186, v0
	s_load_dword s3, s[0:1], 0x38
	s_mov_b64 s[4:5], -1
	s_waitcnt lgkmcnt(0)
	s_cmp_lt_i32 s2, s3
	s_cbranch_scc1 .LBB2_2
	s_sub_i32 s3, s2, s3
	s_cmp_gt_u32 s3, 255
	s_cbranch_scc1 .LBB2_14
	s_load_dwordx4 s[4:7], s[0:1], 0x40
	v_lshrrev_b32_e32 v1, 8, v0
	v_and_b32_e32 v2, 0xff, v0
	v_and_b32_e32 v3, 63, v0
	v_readfirstlane_b32 s8, v1
	v_bfe_u32 v4, v0, 6, 2
	s_lshl_b32 s9, s3, 1
	s_nop 1
	s_add_u32 s9, s9, s8
	s_lshr_b32 s10, s9, 8
	s_bfe_u32 s11, s9, 0x40004
	s_and_b32 s12, s9, 15
	s_lshl_b32 s13, s11, 6
	s_lshl_b32 s14, s12, 6
	s_mul_i32 s15, s10, 0x3d2844
	s_movk_i32 s24, 0x3e9
	s_waitcnt lgkmcnt(0)
	s_add_u32 s16, s4, s15
	s_addc_u32 s17, s5, 0
	s_add_u32 s18, s16, 0x7a5088
	s_addc_u32 s19, s17, 0
	s_lshl_b32 s15, s10, 21
	s_add_u32 s20, s6, s15
	s_addc_u32 s21, s7, 0
	s_add_u32 s20, s20, 0x800000
	s_addc_u32 s21, s21, 0
	s_add_u32 s22, s20, 0x400000
	s_addc_u32 s23, s21, 0
	v_add_u32_e32 v5, s13, v4
	v_add_u32_e32 v6, s14, v3
	v_cmp_gt_u32_e64 s[28:29], s24, v6
	v_min_u32_e32 v6, 0x3e8, v6
	v_lshlrev_b32_e32 v6, 2, v6
	v_min_u32_e32 v7, 0x3e8, v5
	v_mul_u32_u24_e32 v7, 0xfa4, v7
	v_add_u32_e32 v48, v7, v6
	v_add_u32_e32 v7, 4, v5
	v_min_u32_e32 v7, 0x3e8, v7
	v_mul_u32_u24_e32 v7, 0xfa4, v7
	v_add_u32_e32 v49, v7, v6
	v_add_u32_e32 v7, 8, v5
	v_min_u32_e32 v7, 0x3e8, v7
	v_mul_u32_u24_e32 v7, 0xfa4, v7
	v_add_u32_e32 v50, v7, v6
	v_add_u32_e32 v7, 12, v5
	v_min_u32_e32 v7, 0x3e8, v7
	v_mul_u32_u24_e32 v7, 0xfa4, v7
	v_add_u32_e32 v51, v7, v6
	v_add_u32_e32 v7, 16, v5
	v_min_u32_e32 v7, 0x3e8, v7
	v_mul_u32_u24_e32 v7, 0xfa4, v7
	v_add_u32_e32 v52, v7, v6
	v_add_u32_e32 v7, 20, v5
	v_min_u32_e32 v7, 0x3e8, v7
	v_mul_u32_u24_e32 v7, 0xfa4, v7
	v_add_u32_e32 v53, v7, v6
	v_add_u32_e32 v7, 24, v5
	v_min_u32_e32 v7, 0x3e8, v7
	v_mul_u32_u24_e32 v7, 0xfa4, v7
	v_add_u32_e32 v54, v7, v6
	v_add_u32_e32 v7, 28, v5
	v_min_u32_e32 v7, 0x3e8, v7
	v_mul_u32_u24_e32 v7, 0xfa4, v7
	v_add_u32_e32 v55, v7, v6
	v_add_u32_e32 v7, 32, v5
	v_min_u32_e32 v7, 0x3e8, v7
	v_mul_u32_u24_e32 v7, 0xfa4, v7
	v_add_u32_e32 v56, v7, v6
	v_add_u32_e32 v7, 36, v5
	v_min_u32_e32 v7, 0x3e8, v7
	v_mul_u32_u24_e32 v7, 0xfa4, v7
	v_add_u32_e32 v57, v7, v6
	v_add_u32_e32 v7, 40, v5
	v_min_u32_e32 v7, 0x3e8, v7
	v_mul_u32_u24_e32 v7, 0xfa4, v7
	v_add_u32_e32 v58, v7, v6
	v_add_u32_e32 v7, 44, v5
	v_min_u32_e32 v7, 0x3e8, v7
	v_mul_u32_u24_e32 v7, 0xfa4, v7
	v_add_u32_e32 v59, v7, v6
	v_add_u32_e32 v7, 48, v5
	v_min_u32_e32 v7, 0x3e8, v7
	v_mul_u32_u24_e32 v7, 0xfa4, v7
	v_add_u32_e32 v60, v7, v6
	v_add_u32_e32 v7, 52, v5
	v_min_u32_e32 v7, 0x3e8, v7
	v_mul_u32_u24_e32 v7, 0xfa4, v7
	v_add_u32_e32 v61, v7, v6
	v_add_u32_e32 v7, 56, v5
	v_min_u32_e32 v7, 0x3e8, v7
	v_mul_u32_u24_e32 v7, 0xfa4, v7
	v_add_u32_e32 v62, v7, v6
	v_add_u32_e32 v7, 60, v5
	v_min_u32_e32 v7, 0x3e8, v7
	v_mul_u32_u24_e32 v7, 0xfa4, v7
	v_add_u32_e32 v63, v7, v6
	global_load_dword v16, v48, s[16:17] nt
	global_load_dword v17, v49, s[16:17] nt
	global_load_dword v18, v50, s[16:17] nt
	global_load_dword v19, v51, s[16:17] nt
	global_load_dword v20, v52, s[16:17] nt
	global_load_dword v21, v53, s[16:17] nt
	global_load_dword v22, v54, s[16:17] nt
	global_load_dword v23, v55, s[16:17] nt
	global_load_dword v24, v56, s[16:17] nt
	global_load_dword v25, v57, s[16:17] nt
	global_load_dword v26, v58, s[16:17] nt
	global_load_dword v27, v59, s[16:17] nt
	global_load_dword v28, v60, s[16:17] nt
	global_load_dword v29, v61, s[16:17] nt
	global_load_dword v30, v62, s[16:17] nt
	global_load_dword v31, v63, s[16:17] nt
	global_load_dword v32, v48, s[18:19] nt
	global_load_dword v33, v49, s[18:19] nt
	global_load_dword v34, v50, s[18:19] nt
	global_load_dword v35, v51, s[18:19] nt
	global_load_dword v36, v52, s[18:19] nt
	global_load_dword v37, v53, s[18:19] nt
	global_load_dword v38, v54, s[18:19] nt
	global_load_dword v39, v55, s[18:19] nt
	global_load_dword v40, v56, s[18:19] nt
	global_load_dword v41, v57, s[18:19] nt
	global_load_dword v42, v58, s[18:19] nt
	global_load_dword v43, v59, s[18:19] nt
	global_load_dword v44, v60, s[18:19] nt
	global_load_dword v45, v61, s[18:19] nt
	global_load_dword v46, v62, s[18:19] nt
	global_load_dword v47, v63, s[18:19] nt
	v_mul_u32_u24_e32 v8, 65, v4
	v_add_u32_e32 v8, v8, v3
	v_lshlrev_b32_e32 v8, 2, v8
	s_mul_i32 s25, s8, 0x4100
	v_add_u32_e32 v8, s25, v8
	v_and_b32_e32 v9, 7, v2
	v_lshrrev_b32_e32 v10, 3, v2
	v_mul_u32_u24_e32 v11, 0x208, v9
	v_add_u32_e32 v11, v11, v10
	v_lshlrev_b32_e32 v11, 2, v11
	v_add_u32_e32 v11, s25, v11
	v_add_u32_e32 v12, s14, v10
	v_lshlrev_b32_e32 v12, 11, v12
	v_lshlrev_b32_e32 v13, 4, v9
	v_add_u32_e32 v12, v12, v13
	s_lshl_b32 s26, s13, 1
	v_add_u32_e32 v12, s26, v12
	v_add_u32_e32 v14, 0x10000, v12
	s_waitcnt vmcnt(31)
	v_cmp_gt_u32_e32 vcc, s24, v5
	s_and_b64 vcc, vcc, s[28:29]
	s_nop 1
	v_cndmask_b32_e32 v7, 0, v16, vcc
	ds_write_b32 v8, v7
	s_waitcnt vmcnt(30)
	v_add_u32_e32 v7, 4, v5
	v_cmp_gt_u32_e32 vcc, s24, v7
	s_and_b64 vcc, vcc, s[28:29]
	s_nop 1
	v_cndmask_b32_e32 v7, 0, v17, vcc
	ds_write_b32 v8, v7 offset:1040
	s_waitcnt vmcnt(29)
	v_add_u32_e32 v7, 8, v5
	v_cmp_gt_u32_e32 vcc, s24, v7
	s_and_b64 vcc, vcc, s[28:29]
	s_nop 1
	v_cndmask_b32_e32 v7, 0, v18, vcc
	ds_write_b32 v8, v7 offset:2080
	s_waitcnt vmcnt(28)
	v_add_u32_e32 v7, 12, v5
	v_cmp_gt_u32_e32 vcc, s24, v7
	s_and_b64 vcc, vcc, s[28:29]
	s_nop 1
	v_cndmask_b32_e32 v7, 0, v19, vcc
	ds_write_b32 v8, v7 offset:3120
	s_waitcnt vmcnt(27)
	v_add_u32_e32 v7, 16, v5
	v_cmp_gt_u32_e32 vcc, s24, v7
	s_and_b64 vcc, vcc, s[28:29]
	s_nop 1
	v_cndmask_b32_e32 v7, 0, v20, vcc
	ds_write_b32 v8, v7 offset:4160
	s_waitcnt vmcnt(26)
	v_add_u32_e32 v7, 20, v5
	v_cmp_gt_u32_e32 vcc, s24, v7
	s_and_b64 vcc, vcc, s[28:29]
	s_nop 1
	v_cndmask_b32_e32 v7, 0, v21, vcc
	ds_write_b32 v8, v7 offset:5200
	s_waitcnt vmcnt(25)
	v_add_u32_e32 v7, 24, v5
	v_cmp_gt_u32_e32 vcc, s24, v7
	s_and_b64 vcc, vcc, s[28:29]
	s_nop 1
	v_cndmask_b32_e32 v7, 0, v22, vcc
	ds_write_b32 v8, v7 offset:6240
	s_waitcnt vmcnt(24)
	v_add_u32_e32 v7, 28, v5
	v_cmp_gt_u32_e32 vcc, s24, v7
	s_and_b64 vcc, vcc, s[28:29]
	s_nop 1
	v_cndmask_b32_e32 v7, 0, v23, vcc
	ds_write_b32 v8, v7 offset:7280
	s_waitcnt vmcnt(23)
	v_add_u32_e32 v7, 32, v5
	v_cmp_gt_u32_e32 vcc, s24, v7
	s_and_b64 vcc, vcc, s[28:29]
	s_nop 1
	v_cndmask_b32_e32 v7, 0, v24, vcc
	ds_write_b32 v8, v7 offset:8320
	s_waitcnt vmcnt(22)
	v_add_u32_e32 v7, 36, v5
	v_cmp_gt_u32_e32 vcc, s24, v7
	s_and_b64 vcc, vcc, s[28:29]
	s_nop 1
	v_cndmask_b32_e32 v7, 0, v25, vcc
	ds_write_b32 v8, v7 offset:9360
	s_waitcnt vmcnt(21)
	v_add_u32_e32 v7, 40, v5
	v_cmp_gt_u32_e32 vcc, s24, v7
	s_and_b64 vcc, vcc, s[28:29]
	s_nop 1
	v_cndmask_b32_e32 v7, 0, v26, vcc
	ds_write_b32 v8, v7 offset:10400
	s_waitcnt vmcnt(20)
	v_add_u32_e32 v7, 44, v5
	v_cmp_gt_u32_e32 vcc, s24, v7
	s_and_b64 vcc, vcc, s[28:29]
	s_nop 1
	v_cndmask_b32_e32 v7, 0, v27, vcc
	ds_write_b32 v8, v7 offset:11440
	s_waitcnt vmcnt(19)
	v_add_u32_e32 v7, 48, v5
	v_cmp_gt_u32_e32 vcc, s24, v7
	s_and_b64 vcc, vcc, s[28:29]
	s_nop 1
	v_cndmask_b32_e32 v7, 0, v28, vcc
	ds_write_b32 v8, v7 offset:12480
	s_waitcnt vmcnt(18)
	v_add_u32_e32 v7, 52, v5
	v_cmp_gt_u32_e32 vcc, s24, v7
	s_and_b64 vcc, vcc, s[28:29]
	s_nop 1
	v_cndmask_b32_e32 v7, 0, v29, vcc
	ds_write_b32 v8, v7 offset:13520
	s_waitcnt vmcnt(17)
	v_add_u32_e32 v7, 56, v5
	v_cmp_gt_u32_e32 vcc, s24, v7
	s_and_b64 vcc, vcc, s[28:29]
	s_nop 1
	v_cndmask_b32_e32 v7, 0, v30, vcc
	ds_write_b32 v8, v7 offset:14560
	s_waitcnt vmcnt(16)
	v_add_u32_e32 v7, 60, v5
	v_cmp_gt_u32_e32 vcc, s24, v7
	s_and_b64 vcc, vcc, s[28:29]
	s_nop 1
	v_cndmask_b32_e32 v7, 0, v31, vcc
	ds_write_b32 v8, v7 offset:15600
	s_waitcnt lgkmcnt(0)
	s_barrier
	ds_read_b32 v64, v11
	ds_read_b32 v65, v11 offset:260
	ds_read_b32 v66, v11 offset:520
	ds_read_b32 v67, v11 offset:780
	ds_read_b32 v68, v11 offset:1040
	ds_read_b32 v69, v11 offset:1300
	ds_read_b32 v70, v11 offset:1560
	ds_read_b32 v71, v11 offset:1820
	ds_read_b32 v72, v11 offset:128
	ds_read_b32 v73, v11 offset:388
	ds_read_b32 v74, v11 offset:648
	ds_read_b32 v75, v11 offset:908
	s_waitcnt lgkmcnt(4)
	ds_read_b32 v76, v11 offset:1168
	ds_read_b32 v77, v11 offset:1428
	ds_read_b32 v78, v11 offset:1688
	ds_read_b32 v79, v11 offset:1948
	s_waitcnt lgkmcnt(0)
	v_cvt_pk_f16_f32 v80, v64, v65
	v_cvt_pk_f16_f32 v81, v66, v67
	v_cvt_pk_f16_f32 v82, v68, v69
	v_cvt_pk_f16_f32 v83, v70, v71
	v_cvt_pk_f16_f32 v84, v72, v73
	v_cvt_pk_f16_f32 v85, v74, v75
	v_cvt_pk_f16_f32 v86, v76, v77
	v_cvt_pk_f16_f32 v87, v78, v79
	global_store_dwordx4 v12, v[80:83], s[20:21]
	global_store_dwordx4 v14, v[84:87], s[20:21]
	s_barrier
	s_waitcnt vmcnt(17)
	v_cmp_gt_u32_e32 vcc, s24, v5
	s_and_b64 vcc, vcc, s[28:29]
	s_nop 1
	v_cndmask_b32_e32 v7, 0, v32, vcc
	ds_write_b32 v8, v7
	s_waitcnt vmcnt(16)
	v_add_u32_e32 v7, 4, v5
	v_cmp_gt_u32_e32 vcc, s24, v7
	s_and_b64 vcc, vcc, s[28:29]
	s_nop 1
	v_cndmask_b32_e32 v7, 0, v33, vcc
	ds_write_b32 v8, v7 offset:1040
	s_waitcnt vmcnt(15)
	v_add_u32_e32 v7, 8, v5
	v_cmp_gt_u32_e32 vcc, s24, v7
	s_and_b64 vcc, vcc, s[28:29]
	s_nop 1
	v_cndmask_b32_e32 v7, 0, v34, vcc
	ds_write_b32 v8, v7 offset:2080
	s_waitcnt vmcnt(14)
	v_add_u32_e32 v7, 12, v5
	v_cmp_gt_u32_e32 vcc, s24, v7
	s_and_b64 vcc, vcc, s[28:29]
	s_nop 1
	v_cndmask_b32_e32 v7, 0, v35, vcc
	ds_write_b32 v8, v7 offset:3120
	s_waitcnt vmcnt(13)
	v_add_u32_e32 v7, 16, v5
	v_cmp_gt_u32_e32 vcc, s24, v7
	s_and_b64 vcc, vcc, s[28:29]
	s_nop 1
	v_cndmask_b32_e32 v7, 0, v36, vcc
	ds_write_b32 v8, v7 offset:4160
	s_waitcnt vmcnt(12)
	v_add_u32_e32 v7, 20, v5
	v_cmp_gt_u32_e32 vcc, s24, v7
	s_and_b64 vcc, vcc, s[28:29]
	s_nop 1
	v_cndmask_b32_e32 v7, 0, v37, vcc
	ds_write_b32 v8, v7 offset:5200
	s_waitcnt vmcnt(11)
	v_add_u32_e32 v7, 24, v5
	v_cmp_gt_u32_e32 vcc, s24, v7
	s_and_b64 vcc, vcc, s[28:29]
	s_nop 1
	v_cndmask_b32_e32 v7, 0, v38, vcc
	ds_write_b32 v8, v7 offset:6240
	s_waitcnt vmcnt(10)
	v_add_u32_e32 v7, 28, v5
	v_cmp_gt_u32_e32 vcc, s24, v7
	s_and_b64 vcc, vcc, s[28:29]
	s_nop 1
	v_cndmask_b32_e32 v7, 0, v39, vcc
	ds_write_b32 v8, v7 offset:7280
	s_waitcnt vmcnt(9)
	v_add_u32_e32 v7, 32, v5
	v_cmp_gt_u32_e32 vcc, s24, v7
	s_and_b64 vcc, vcc, s[28:29]
	s_nop 1
	v_cndmask_b32_e32 v7, 0, v40, vcc
	ds_write_b32 v8, v7 offset:8320
	s_waitcnt vmcnt(8)
	v_add_u32_e32 v7, 36, v5
	v_cmp_gt_u32_e32 vcc, s24, v7
	s_and_b64 vcc, vcc, s[28:29]
	s_nop 1
	v_cndmask_b32_e32 v7, 0, v41, vcc
	ds_write_b32 v8, v7 offset:9360
	s_waitcnt vmcnt(7)
	v_add_u32_e32 v7, 40, v5
	v_cmp_gt_u32_e32 vcc, s24, v7
	s_and_b64 vcc, vcc, s[28:29]
	s_nop 1
	v_cndmask_b32_e32 v7, 0, v42, vcc
	ds_write_b32 v8, v7 offset:10400
	s_waitcnt vmcnt(6)
	v_add_u32_e32 v7, 44, v5
	v_cmp_gt_u32_e32 vcc, s24, v7
	s_and_b64 vcc, vcc, s[28:29]
	s_nop 1
	v_cndmask_b32_e32 v7, 0, v43, vcc
	ds_write_b32 v8, v7 offset:11440
	s_waitcnt vmcnt(5)
	v_add_u32_e32 v7, 48, v5
	v_cmp_gt_u32_e32 vcc, s24, v7
	s_and_b64 vcc, vcc, s[28:29]
	s_nop 1
	v_cndmask_b32_e32 v7, 0, v44, vcc
	ds_write_b32 v8, v7 offset:12480
	s_waitcnt vmcnt(4)
	v_add_u32_e32 v7, 52, v5
	v_cmp_gt_u32_e32 vcc, s24, v7
	s_and_b64 vcc, vcc, s[28:29]
	s_nop 1
	v_cndmask_b32_e32 v7, 0, v45, vcc
	ds_write_b32 v8, v7 offset:13520
	s_waitcnt vmcnt(3)
	v_add_u32_e32 v7, 56, v5
	v_cmp_gt_u32_e32 vcc, s24, v7
	s_and_b64 vcc, vcc, s[28:29]
	s_nop 1
	v_cndmask_b32_e32 v7, 0, v46, vcc
	ds_write_b32 v8, v7 offset:14560
	s_waitcnt vmcnt(2)
	v_add_u32_e32 v7, 60, v5
	v_cmp_gt_u32_e32 vcc, s24, v7
	s_and_b64 vcc, vcc, s[28:29]
	s_nop 1
	v_cndmask_b32_e32 v7, 0, v47, vcc
	ds_write_b32 v8, v7 offset:15600
	s_waitcnt lgkmcnt(0)
	s_barrier
	ds_read_b32 v64, v11
	ds_read_b32 v65, v11 offset:260
	ds_read_b32 v66, v11 offset:520
	ds_read_b32 v67, v11 offset:780
	ds_read_b32 v68, v11 offset:1040
	ds_read_b32 v69, v11 offset:1300
	ds_read_b32 v70, v11 offset:1560
	ds_read_b32 v71, v11 offset:1820
	ds_read_b32 v72, v11 offset:128
	ds_read_b32 v73, v11 offset:388
	ds_read_b32 v74, v11 offset:648
	ds_read_b32 v75, v11 offset:908
	s_waitcnt lgkmcnt(4)
	ds_read_b32 v76, v11 offset:1168
	ds_read_b32 v77, v11 offset:1428
	ds_read_b32 v78, v11 offset:1688
	ds_read_b32 v79, v11 offset:1948
	s_waitcnt lgkmcnt(0)
	v_cvt_pk_f16_f32 v80, v64, v65
	v_cvt_pk_f16_f32 v81, v66, v67
	v_cvt_pk_f16_f32 v82, v68, v69
	v_cvt_pk_f16_f32 v83, v70, v71
	v_cvt_pk_f16_f32 v84, v72, v73
	v_cvt_pk_f16_f32 v85, v74, v75
	v_cvt_pk_f16_f32 v86, v76, v77
	v_cvt_pk_f16_f32 v87, v78, v79
	global_store_dwordx4 v12, v[80:83], s[22:23]
	global_store_dwordx4 v14, v[84:87], s[22:23]
	s_branch .LBB2_14

amdhsa.kernels:
  - .agpr_count:     0
    .args:
      - .actual_access:  read_only
        .address_space:  global
        .offset:         0
        .size:           8
        .value_kind:     global_buffer
      - .actual_access:  read_only
        .address_space:  global
        .offset:         8
        .size:           8
        .value_kind:     global_buffer
      - .actual_access:  read_only
        .address_space:  global
        .offset:         16
        .size:           8
        .value_kind:     global_buffer
      - .actual_access:  read_only
        .address_space:  global
        .offset:         24
        .size:           8
        .value_kind:     global_buffer
      - .actual_access:  read_only
        .address_space:  global
        .offset:         32
        .size:           8
        .value_kind:     global_buffer
      - .actual_access:  read_only
        .address_space:  global
        .offset:         40
        .size:           8
        .value_kind:     global_buffer
      - .actual_access:  read_only
        .address_space:  global
        .offset:         48
        .size:           8
        .value_kind:     global_buffer
      - .actual_access:  read_only
        .address_space:  global
        .offset:         56
        .size:           8
        .value_kind:     global_buffer
      - .actual_access:  write_only
        .address_space:  global
        .offset:         64
        .size:           8
        .value_kind:     global_buffer
    .group_segment_fixed_size: 16832
    .kernarg_segment_align: 8
    .kernarg_segment_size: 72
    .language:       OpenCL C
    .language_version:
      - 2
      - 0
    .max_flat_workgroup_size: 256
    .name:           _Z12front_kernelPKiS0_S0_PKfS2_S2_S2_S2_Pc
    .private_segment_fixed_size: 0
    .sgpr_count:     106
    .sgpr_spill_count: 398
    .symbol:         _Z12front_kernelPKiS0_S0_PKfS2_S2_S2_S2_Pc.kd
    .uniform_work_group_size: 1
    .uses_dynamic_stack: false
    .vgpr_count:     78
    .vgpr_spill_count: 0
    .wavefront_size: 64
  - .agpr_count:     0
    .args:
      - .actual_access:  read_only
        .address_space:  global
        .offset:         0
        .size:           8
        .value_kind:     global_buffer
      - .actual_access:  read_only
        .address_space:  global
        .offset:         8
        .size:           8
        .value_kind:     global_buffer
      - .actual_access:  read_only
        .address_space:  global
        .offset:         16
        .size:           8
        .value_kind:     global_buffer
      - .actual_access:  write_only
        .address_space:  global
        .offset:         24
        .size:           8
        .value_kind:     global_buffer
    .group_segment_fixed_size: 0
    .kernarg_segment_align: 8
    .kernarg_segment_size: 32
    .language:       OpenCL C
    .language_version:
      - 2
      - 0
    .max_flat_workgroup_size: 256
    .name:           _Z12final_kernelPKDF16_PKfS2_Pf
    .private_segment_fixed_size: 0
    .sgpr_count:     14
    .sgpr_spill_count: 0
    .symbol:         _Z12final_kernelPKDF16_PKfS2_Pf.kd
    .uniform_work_group_size: 1
    .uses_dynamic_stack: false
    .vgpr_count:     64
    .vgpr_spill_count: 0
    .wavefront_size: 64
  - .agpr_count:     0
    .args:
      - .address_space:  global
        .offset:         0
        .size:           8
        .value_kind:     global_buffer
      - .actual_access:  write_only
        .address_space:  global
        .offset:         8
        .size:           8
        .value_kind:     global_buffer
      - .actual_access:  read_only
        .address_space:  global
        .offset:         16
        .size:           8
        .value_kind:     global_buffer
      - .actual_access:  read_only
        .address_space:  global
        .offset:         24
        .size:           8
        .value_kind:     global_buffer
      - .address_space:  global
        .offset:         32
        .size:           8
        .value_kind:     global_buffer
      - .address_space:  global
        .offset:         40
        .size:           8
        .value_kind:     global_buffer
      - .actual_access:  read_only
        .address_space:  global
        .offset:         48
        .size:           8
        .value_kind:     global_buffer
      - .offset:         56
        .size:           4
        .value_kind:     by_value
      - .actual_access:  read_only
        .address_space:  global
        .offset:         64
        .size:           8
        .value_kind:     global_buffer
      - .actual_access:  write_only
        .address_space:  global
        .offset:         72
        .size:           8
        .value_kind:     global_buffer
    .group_segment_fixed_size: 0
    .kernarg_segment_align: 8
    .kernarg_segment_size: 80
    .language:       OpenCL C
    .language_version:
      - 2
      - 0
    .max_flat_workgroup_size: 512
    .name:           _Z16gemm_glds_kernelILi2EEvPKDF16_PDF16_PKiS4_S1_S1_PKfiS6_Pc
    .private_segment_fixed_size: 0
    .sgpr_count:     50
    .sgpr_spill_count: 0
    .symbol:         _Z16gemm_glds_kernelILi2EEvPKDF16_PDF16_PKiS4_S1_S1_PKfiS6_Pc.kd
    .uniform_work_group_size: 1
    .uses_dynamic_stack: false
    .vgpr_count:     188
    .vgpr_spill_count: 0
    .wavefront_size: 64
  - .agpr_count:     0
    .args:
      - .actual_access:  read_only
        .address_space:  global
        .offset:         0
        .size:           8
        .value_kind:     global_buffer
      - .actual_access:  write_only
        .address_space:  global
        .offset:         8
        .size:           8
        .value_kind:     global_buffer
      - .actual_access:  read_only
        .address_space:  global
        .offset:         16
        .size:           8
        .value_kind:     global_buffer
      - .actual_access:  read_only
        .address_space:  global
        .offset:         24
        .size:           8
        .value_kind:     global_buffer
      - .actual_access:  read_only
        .address_space:  global
        .offset:         32
        .size:           8
        .value_kind:     global_buffer
      - .actual_access:  read_only
        .address_space:  global
        .offset:         40
        .size:           8
        .value_kind:     global_buffer
      - .actual_access:  read_only
        .address_space:  global
        .offset:         48
        .size:           8
        .value_kind:     global_buffer
    .group_segment_fixed_size: 0
    .kernarg_segment_align: 8
    .kernarg_segment_size: 56
    .language:       OpenCL C
    .language_version:
      - 2
      - 0
    .max_flat_workgroup_size: 512
    .name:           _Z11gemm_kernelILi0ELi192ELi256ELi128ELi2ELi4ELi2ELi2ELi64EEvPKDF16_PDF16_PKiS4_S1_S1_PKf
    .private_segment_fixed_size: 0
    .sgpr_count:     30
    .sgpr_spill_count: 0
    .symbol:         _Z11gemm_kernelILi0ELi192ELi256ELi128ELi2ELi4ELi2ELi2ELi64EEvPKDF16_PDF16_PKiS4_S1_S1_PKf.kd
    .uniform_work_group_size: 1
    .uses_dynamic_stack: false
    .vgpr_count:     254
    .vgpr_spill_count: 0
    .wavefront_size: 64
  - .agpr_count:     0
    .args:
      - .actual_access:  read_only
        .address_space:  global
        .offset:         0
        .size:           8
        .value_kind:     global_buffer
      - .actual_access:  write_only
        .address_space:  global
        .offset:         8
        .size:           8
        .value_kind:     global_buffer
      - .actual_access:  read_only
        .address_space:  global
        .offset:         16
        .size:           8
        .value_kind:     global_buffer
      - .actual_access:  read_only
        .address_space:  global
        .offset:         24
        .size:           8
        .value_kind:     global_buffer
      - .actual_access:  read_only
        .address_space:  global
        .offset:         32
        .size:           8
        .value_kind:     global_buffer
      - .actual_access:  read_only
        .address_space:  global
        .offset:         40
        .size:           8
        .value_kind:     global_buffer
      - .actual_access:  read_only
        .address_space:  global
        .offset:         48
        .size:           8
        .value_kind:     global_buffer
    .group_segment_fixed_size: 0
    .kernarg_segment_align: 8
    .kernarg_segment_size: 56
    .language:       OpenCL C
    .language_version:
      - 2
      - 0
    .max_flat_workgroup_size: 512
    .name:           _Z11gemm_kernelILi0ELi96ELi256ELi128ELi2ELi4ELi2ELi2ELi64EEvPKDF16_PDF16_PKiS4_S1_S1_PKf
    .private_segment_fixed_size: 0
    .sgpr_count:     32
    .sgpr_spill_count: 0
    .symbol:         _Z11gemm_kernelILi0ELi96ELi256ELi128ELi2ELi4ELi2ELi2ELi64EEvPKDF16_PDF16_PKiS4_S1_S1_PKf.kd
    .uniform_work_group_size: 1
    .uses_dynamic_stack: false
    .vgpr_count:     224
    .vgpr_spill_count: 0
    .wavefront_size: 64
  - .agpr_count:     0
    .args:
      - .address_space:  global
        .offset:         0
        .size:           8
        .value_kind:     global_buffer
      - .actual_access:  write_only
        .address_space:  global
        .offset:         8
        .size:           8
        .value_kind:     global_buffer
      - .actual_access:  read_only
        .address_space:  global
        .offset:         16
        .size:           8
        .value_kind:     global_buffer
      - .actual_access:  read_only
        .address_space:  global
        .offset:         24
        .size:           8
        .value_kind:     global_buffer
      - .address_space:  global
        .offset:         32
        .size:           8
        .value_kind:     global_buffer
      - .address_space:  global
        .offset:         40
        .size:           8
        .value_kind:     global_buffer
      - .actual_access:  read_only
        .address_space:  global
        .offset:         48
        .size:           8
        .value_kind:     global_buffer
    .group_segment_fixed_size: 0
    .kernarg_segment_align: 8
    .kernarg_segment_size: 56
    .language:       OpenCL C
    .language_version:
      - 2
      - 0
    .max_flat_workgroup_size: 256
    .name:           _Z15gemm_dma_kernelILi0ELi96ELi128ELi64ELi2ELi2ELi3EEvPKDF16_PDF16_PKiS4_S1_S1_PKf
    .private_segment_fixed_size: 0
    .sgpr_count:     33
    .sgpr_spill_count: 0
    .symbol:         _Z15gemm_dma_kernelILi0ELi96ELi128ELi64ELi2ELi2ELi3EEvPKDF16_PDF16_PKiS4_S1_S1_PKf.kd
    .uniform_work_group_size: 1
    .uses_dynamic_stack: false
    .vgpr_count:     224
    .vgpr_spill_count: 0
    .wavefront_size: 64
  - .agpr_count:     0
    .args:
      - .actual_access:  read_only
        .address_space:  global
        .offset:         0
        .size:           8
        .value_kind:     global_buffer
      - .actual_access:  write_only
        .address_space:  global
        .offset:         8
        .size:           8
        .value_kind:     global_buffer
      - .actual_access:  read_only
        .address_space:  global
        .offset:         16
        .size:           8
        .value_kind:     global_buffer
      - .actual_access:  read_only
        .address_space:  global
        .offset:         24
        .size:           8
        .value_kind:     global_buffer
      - .actual_access:  read_only
        .address_space:  global
        .offset:         32
        .size:           8
        .value_kind:     global_buffer
      - .actual_access:  read_only
        .address_space:  global
        .offset:         40
        .size:           8
        .value_kind:     global_buffer
      - .actual_access:  read_only
        .address_space:  global
        .offset:         48
        .size:           8
        .value_kind:     global_buffer
    .group_segment_fixed_size: 0
    .kernarg_segment_align: 8
    .kernarg_segment_size: 56
    .language:       OpenCL C
    .language_version:
      - 2
      - 0
    .max_flat_workgroup_size: 256
    .name:           _Z11gemm_kernelILi0ELi48ELi128ELi64ELi1ELi4ELi2ELi2ELi128EEvPKDF16_PDF16_PKiS4_S1_S1_PKf
    .private_segment_fixed_size: 0
    .sgpr_count:     30
    .sgpr_spill_count: 0
    .symbol:         _Z11gemm_kernelILi0ELi48ELi128ELi64ELi1ELi4ELi2ELi2ELi128EEvPKDF16_PDF16_PKiS4_S1_S1_PKf.kd
    .uniform_work_group_size: 1
    .uses_dynamic_stack: false
    .vgpr_count:     224
    .vgpr_spill_count: 0
    .wavefront_size: 64
  - .agpr_count:     0
    .args:
      - .actual_access:  read_only
        .address_space:  global
        .offset:         0
        .size:           8
        .value_kind:     global_buffer
      - .actual_access:  write_only
        .address_space:  global
        .offset:         8
        .size:           8
        .value_kind:     global_buffer
      - .actual_access:  read_only
        .address_space:  global
        .offset:         16
        .size:           8
        .value_kind:     global_buffer
      - .actual_access:  read_only
        .address_space:  global
        .offset:         24
        .size:           8
        .value_kind:     global_buffer
      - .actual_access:  read_only
        .address_space:  global
        .offset:         32
        .size:           8
        .value_kind:     global_buffer
      - .actual_access:  read_only
        .address_space:  global
        .offset:         40
        .size:           8
        .value_kind:     global_buffer
      - .actual_access:  read_only
        .address_space:  global
        .offset:         48
        .size:           8
        .value_kind:     global_buffer
    .group_segment_fixed_size: 0
    .kernarg_segment_align: 8
    .kernarg_segment_size: 56
    .language:       OpenCL C
    .language_version:
      - 2
      - 0
    .max_flat_workgroup_size: 512
    .name:           _Z11gemm_kernelILi1ELi64ELi128ELi128ELi2ELi4ELi2ELi2ELi128EEvPKDF16_PDF16_PKiS4_S1_S1_PKf
    .private_segment_fixed_size: 0
    .sgpr_count:     23
    .sgpr_spill_count: 0
    .symbol:         _Z11gemm_kernelILi1ELi64ELi128ELi128ELi2ELi4ELi2ELi2ELi128EEvPKDF16_PDF16_PKiS4_S1_S1_PKf.kd
    .uniform_work_group_size: 1
    .uses_dynamic_stack: false
    .vgpr_count:     224
    .vgpr_spill_count: 0
    .wavefront_size: 64
